# gating units rebalanced to 2 per workgroup (attention units are uniformly short after the early exit), on top of v058
# baseline (speedup 1.0000x reference)
.LBB0_690:
	s_mov_b32 s2, 0x22222222
	s_lshl_b32 s6, s52, 2
	s_mov_b32 s3, 0x22222222
	s_lshr_b64 s[2:3], s[2:3], s6
	s_and_b32 s2, s2, 7
	s_cmp_eq_u32 s2, 0
	s_cbranch_scc1 .LBB0_705
	s_cmp_lt_i32 s52, 8
	s_mov_b32 s3, 0xe0c0a08
	s_cselect_b32 s7, s3, 0x1e1c1a18
	s_mov_b32 s6, 0x6040200
	s_cselect_b32 s6, s6, 0x16141210
	s_lshl_b32 s3, s52, 3
	s_lshr_b64 s[6:7], s[6:7], s3
	s_and_b32 s10, s33, 0x380
	v_readlane_b32 s16, v254, 18
	s_and_b32 s3, s6, 31
	s_and_b32 s12, s8, 8
	s_lshl_b32 s6, s10, 2
	v_readlane_b32 s18, v254, 20
	v_readlane_b32 s19, v254, 21
	s_add_u32 s6, s18, s6
	s_addc_u32 s7, s19, 0
	s_waitcnt vmcnt(15)
	v_lshlrev_b32_e32 v2, 2, v76
	global_load_dwordx4 v[34:37], v2, s[6:7]
	global_load_dwordx4 v[38:41], v2, s[6:7] offset:16
	global_load_dwordx4 v[42:45], v2, s[6:7] offset:32
	global_load_dwordx4 v[46:49], v2, s[6:7] offset:48
	global_load_dwordx4 v[50:53], v2, s[6:7] offset:64
	global_load_dwordx4 v[54:57], v2, s[6:7] offset:80
	global_load_dwordx4 v[58:61], v2, s[6:7] offset:96
	global_load_dwordx4 v[62:65], v2, s[6:7] offset:112
	s_lshl_b32 s11, s2, 8
	s_lshl_b32 s2, s3, 4
	v_readlane_b32 s17, v254, 19
	v_readlane_b32 s20, v254, 22
	v_readlane_b32 s21, v254, 23
	v_readlane_b32 s22, v254, 24
	v_readlane_b32 s23, v254, 25
	v_readlane_b32 s24, v254, 26
	v_readlane_b32 s25, v254, 27
	v_readlane_b32 s26, v254, 28
	v_readlane_b32 s27, v254, 29
	v_readlane_b32 s28, v254, 30
	v_readlane_b32 s29, v254, 31
	v_readlane_b32 s30, v254, 32
	v_readlane_b32 s31, v254, 33
	s_or_b32 s2, s2, s12
	s_lshr_b32 s6, s2, 3
	v_readlane_b32 s16, v254, 38
	s_lshl_b32 s12, s6, 7
	s_lshl_b32 s2, s6, 11
	v_readlane_b32 s30, v254, 52
	v_readlane_b32 s31, v254, 53
	s_add_u32 s2, s30, s2
	v_lshlrev_b32_e32 v74, 4, v78
	v_mov_b32_e32 v75, 0
	s_addc_u32 s3, s31, 0
	v_lshl_add_u64 v[2:3], s[2:3], 0, v[74:75]
	s_mov_b64 s[2:3], 0x200000
	v_lshl_add_u64 v[76:77], v[2:3], 0, s[2:3]
	v_lshlrev_b32_e32 v2, 11, v78
	s_and_b32 s2, s8, 7
	v_and_b32_e32 v3, 3, v0
	v_lshl_or_b32 v2, s6, 18, v2
	s_lshl_b32 s2, s2, 8
	v_lshlrev_b32_e32 v3, 6, v3
	v_or3_b32 v74, v2, s2, v3
	v_lshl_add_u64 v[2:3], s[30:31], 0, v[74:75]
	s_mov_b64 s[2:3], 0x3b200020
	v_or_b32_e32 v71, s10, v216
	v_add_u32_e32 v85, 0, v70
	v_lshl_add_u64 v[78:79], v[2:3], 0, s[2:3]
	s_mov_b64 s[6:7], 0
	v_mov_b32_e32 v86, 0x358637bd
	s_mov_b32 s13, 0xf800000
	v_mov_b32_e32 v87, 0x260
	s_movk_i32 s16, 0x110
	s_mov_b64 s[34:35], 0x800
	s_mov_b64 s[56:57], 0x840
	s_mov_b64 s[72:73], 0x1000
	s_mov_b64 s[74:75], 0x1040
	s_mov_b64 s[78:79], 0x1800
	s_mov_b64 s[80:81], 0x1840
	s_mov_b64 s[82:83], 0x80000
	v_add_u32_e32 v88, v80, v81
	v_readlane_b32 s17, v254, 39
	v_readlane_b32 s18, v254, 40
	v_readlane_b32 s19, v254, 41
	v_readlane_b32 s20, v254, 42
	v_readlane_b32 s21, v254, 43
	v_readlane_b32 s22, v254, 44
	v_readlane_b32 s23, v254, 45
	v_readlane_b32 s24, v254, 46
	v_readlane_b32 s25, v254, 47
	v_readlane_b32 s26, v254, 48
	v_readlane_b32 s27, v254, 49
	v_readlane_b32 s28, v254, 50
	v_readlane_b32 s29, v254, 51
	s_branch .LBB0_693

.LBB0_2258:
	s_mov_b32 s2, 0x22222222
	s_lshl_b32 s6, s16, 2
	s_mov_b32 s3, 0x22222222
	s_lshr_b64 s[2:3], s[2:3], s6
	s_and_b32 s2, s2, 7
	v_readlane_b32 s80, v254, 38
	s_cmp_eq_u32 s2, 0
	v_readlane_b32 s81, v254, 39
	v_readlane_b32 s82, v254, 40
	v_readlane_b32 s83, v254, 41
	v_readlane_b32 s84, v254, 42
	v_readlane_b32 s85, v254, 43
	v_readlane_b32 s86, v254, 44
	v_readlane_b32 s87, v254, 45
	v_readlane_b32 s88, v254, 46
	v_readlane_b32 s89, v254, 47
	v_readlane_b32 s90, v254, 48
	v_readlane_b32 s91, v254, 49
	v_readlane_b32 s92, v254, 50
	v_readlane_b32 s93, v254, 51
	v_readlane_b32 s94, v254, 52
	v_readlane_b32 s95, v254, 53
	s_cbranch_scc1 .LBB0_2273
	s_cmp_lt_i32 s16, 8
	s_mov_b32 s3, 0xe0c0a08
	s_cselect_b32 s7, s3, 0x1e1c1a18
	s_mov_b32 s6, 0x6040200
	s_cselect_b32 s6, s6, 0x16141210
	s_lshl_b32 s3, s16, 3
	s_lshr_b64 s[6:7], s[6:7], s3
	v_readlane_b32 s36, v254, 18
	s_and_b32 s3, s6, 31
	s_and_b32 s18, s8, 8
	s_and_b32 s10, s33, 0x380
	v_readlane_b32 s42, v254, 24
	v_readlane_b32 s43, v254, 25
	s_add_u32 s20, s42, 0x1000
	v_readlane_b32 s38, v254, 20
	s_addc_u32 s21, s43, 0
	s_lshl_b32 s11, s10, 2
	v_readlane_b32 s39, v254, 21
	s_add_u32 s16, s38, s11
	s_addc_u32 s17, s39, 0
	v_lshlrev_b32_e32 v74, 2, v76
	v_mov_b32_e32 v75, 0
	s_mov_b64 s[6:7], 0x1000
	s_waitcnt vmcnt(15)
	v_lshl_add_u64 v[2:3], s[16:17], 0, v[74:75]
	s_movk_i32 s11, 0x1000
	v_lshl_add_u64 v[4:5], v[2:3], 0, s[6:7]
	v_add_co_u32_e32 v2, vcc, s11, v2
	s_lshl_b32 s11, s2, 8
	s_nop 0
	v_addc_co_u32_e32 v3, vcc, 0, v3, vcc
	global_load_dwordx4 v[34:37], v[4:5], off offset:16
	global_load_dwordx4 v[38:41], v[4:5], off offset:32
	global_load_dwordx4 v[42:45], v[4:5], off offset:48
	global_load_dwordx4 v[46:49], v[4:5], off offset:64
	global_load_dwordx4 v[50:53], v[4:5], off offset:80
	global_load_dwordx4 v[54:57], v[4:5], off offset:96
	global_load_dwordx4 v[58:61], v[2:3], off
	global_load_dwordx4 v[62:65], v[4:5], off offset:112
	s_lshl_b32 s2, s3, 4
	s_or_b32 s2, s2, s18
	s_lshr_b32 s17, s2, 3
	s_lshl_b32 s16, s17, 7
	s_lshl_b32 s2, s17, 11
	s_add_u32 s2, s94, s2
	v_lshlrev_b32_e32 v74, 4, v78
	s_addc_u32 s3, s95, 0
	v_lshl_add_u64 v[2:3], s[2:3], 0, v[74:75]
	s_mov_b64 s[2:3], 0x200000
	v_lshl_add_u64 v[76:77], v[2:3], 0, s[2:3]
	v_lshlrev_b32_e32 v2, 11, v78
	s_and_b32 s2, s8, 7
	v_and_b32_e32 v3, 3, v0
	v_lshl_or_b32 v2, s17, 18, v2
	s_lshl_b32 s2, s2, 8
	v_lshlrev_b32_e32 v3, 6, v3
	v_or3_b32 v74, v2, s2, v3
	v_lshl_add_u64 v[2:3], s[94:95], 0, v[74:75]
	s_mov_b64 s[2:3], 0x3b200020
	v_or_b32_e32 v71, s10, v216
	v_add_u32_e32 v83, 0, v70
	v_lshl_add_u64 v[78:79], v[2:3], 0, s[2:3]
	s_mov_b64 s[26:27], 0
	v_mov_b32_e32 v84, 0x358637bd
	s_mov_b32 s17, 0xf800000
	v_mov_b32_e32 v85, 0x260
	s_movk_i32 s18, 0x110
	s_mov_b64 s[34:35], 0x800
	s_mov_b64 s[52:53], 0x840
	s_mov_b64 s[54:55], 0x1040
	s_mov_b64 s[58:59], 0x1800
	s_mov_b64 s[68:69], 0x1840
	s_mov_b64 s[76:77], 0x80000
	v_add_u32_e32 v86, v80, v81
	v_readlane_b32 s37, v254, 19
	v_readlane_b32 s40, v254, 22
	v_readlane_b32 s41, v254, 23
	v_readlane_b32 s44, v254, 26
	v_readlane_b32 s45, v254, 27
	v_readlane_b32 s46, v254, 28
	v_readlane_b32 s47, v254, 29
	v_readlane_b32 s48, v254, 30
	v_readlane_b32 s49, v254, 31
	v_readlane_b32 s50, v254, 32
	v_readlane_b32 s51, v254, 33
	s_branch .LBB0_2261
